# stack + attention loops: v_pk_fma_f32 (scale/shift beside MFMAs) split into scalar v_fma_f32 pairs
# speedup vs baseline: 1.0421x; 1.0006x over previous
.LBB0_881:
	v_max_f32_e32 v36, 0xf149f2ca, v2
	v_cndmask_b32_e64 v236, v36, v230, s[0:1]
	v_mul_f32_e32 v2, 0xbe0293ee, v236
	v_cndmask_b32_e64 v2, v2, v228, s[2:3]
	v_fmamk_f32 v20, v20, 0x3e0293ee, v2
	v_exp_f32_e32 v114, v20
	v_sub_f32_e32 v20, 0xf149f2ca, v36
	v_mul_f32_e32 v20, 0x3e0293ee, v20
	v_fmamk_f32 v21, v21, 0x3e0293ee, v2
	v_fmamk_f32 v22, v22, 0x3e0293ee, v2
	v_fmamk_f32 v23, v23, 0x3e0293ee, v2
	v_fmamk_f32 v24, v24, 0x3e0293ee, v2
	v_fmamk_f32 v25, v25, 0x3e0293ee, v2
	v_fmamk_f32 v26, v26, 0x3e0293ee, v2
	v_fmamk_f32 v27, v27, 0x3e0293ee, v2
	v_fmamk_f32 v28, v28, 0x3e0293ee, v2
	v_fmamk_f32 v29, v29, 0x3e0293ee, v2
	v_fmamk_f32 v30, v30, 0x3e0293ee, v2
	v_fmamk_f32 v31, v31, 0x3e0293ee, v2
	v_fmamk_f32 v32, v32, 0x3e0293ee, v2
	v_fmamk_f32 v33, v33, 0x3e0293ee, v2
	v_fmamk_f32 v34, v34, 0x3e0293ee, v2
	v_fmamk_f32 v35, v35, 0x3e0293ee, v2
	v_exp_f32_e32 v20, v20
	v_exp_f32_e32 v115, v21
	v_exp_f32_e32 v116, v22
	v_exp_f32_e32 v117, v23
	v_exp_f32_e32 v118, v24
	v_exp_f32_e32 v119, v25
	v_exp_f32_e32 v120, v26
	v_exp_f32_e32 v121, v27
	v_exp_f32_e32 v122, v28
	v_exp_f32_e32 v123, v29
	v_exp_f32_e32 v124, v30
	v_exp_f32_e32 v125, v31
	v_exp_f32_e32 v126, v32
	v_exp_f32_e32 v127, v33
	v_exp_f32_e32 v128, v34
	v_exp_f32_e32 v129, v35
	v_cndmask_b32_e64 v235, v20, 1.0, s[0:1]
	v_fma_f32 v144, v18, s12, v2
	v_fma_f32 v145, v19, s12, v2
	v_fma_f32 v142, v16, s12, v2
	v_fma_f32 v143, v17, s12, v2
	v_fma_f32 v140, v14, s12, v2
	v_fma_f32 v141, v15, s12, v2
	v_fma_f32 v138, v12, s12, v2
	v_fma_f32 v139, v13, s12, v2
	v_fma_f32 v136, v10, s12, v2
	v_fma_f32 v137, v11, s12, v2
	v_fma_f32 v134, v8, s12, v2
	v_fma_f32 v135, v9, s12, v2
	v_fma_f32 v132, v6, s12, v2
	v_fma_f32 v133, v7, s12, v2
	v_fma_f32 v130, v4, s12, v2
	v_fma_f32 v131, v5, s12, v2
	s_cmp_lt_i32 s61, 3
	v_lshl_add_u32 v232, v215, 2, s64
	s_waitcnt lgkmcnt(0)
	s_barrier
	s_cbranch_scc1 .LBB0_903
	s_add_i32 s0, s10, s63
	v_mov_b32_e32 v217, v3
	v_add_u32_e32 v2, s0, v226
	s_lshl_b32 s0, s61, 6
	v_lshl_add_u64 v[16:17], s[28:29], 0, v[216:217]
	v_lshl_add_u64 v[198:199], s[30:31], 0, v[216:217]
	v_subrev_u32_e32 v201, s0, v2
	s_add_i32 s31, s0, 0xffffff40
	s_lshl_b32 s0, s61, 15
	v_mov_b32_e32 v217, 0
	s_add_i32 s30, s61, -3
	s_add_i32 s2, s0, 0xfffe0000
	s_mov_b32 s34, 3
	v_mov_b32_e32 v66, 0
	v_mov_b32_e32 v67, v217
	v_mov_b32_e32 v68, v217
	v_mov_b32_e32 v69, v217
	v_mov_b32_e32 v70, v217
	v_mov_b32_e32 v71, v217
	v_mov_b32_e32 v72, v217
	v_mov_b32_e32 v73, v217
	v_mov_b32_e32 v74, v217
	v_mov_b32_e32 v75, v217
	v_mov_b32_e32 v76, v217
	v_mov_b32_e32 v77, v217
	v_mov_b32_e32 v78, v217
	v_mov_b32_e32 v79, v217
	v_mov_b32_e32 v80, v217
	v_mov_b32_e32 v81, v217
	v_mov_b32_e32 v50, 0
	v_mov_b32_e32 v51, v217
	v_mov_b32_e32 v52, v217
	v_mov_b32_e32 v53, v217
	v_mov_b32_e32 v54, v217
	v_mov_b32_e32 v55, v217
	v_mov_b32_e32 v56, v217
	v_mov_b32_e32 v57, v217
	v_mov_b32_e32 v58, v217
	v_mov_b32_e32 v59, v217
	v_mov_b32_e32 v60, v217
	v_mov_b32_e32 v61, v217
	v_mov_b32_e32 v62, v217
	v_mov_b32_e32 v63, v217
	v_mov_b32_e32 v64, v217
	v_mov_b32_e32 v65, v217
	v_mov_b32_e32 v34, 0
	v_mov_b32_e32 v35, v217
	v_mov_b32_e32 v36, v217
	v_mov_b32_e32 v37, v217
	v_mov_b32_e32 v38, v217
	v_mov_b32_e32 v39, v217
	v_mov_b32_e32 v40, v217
	v_mov_b32_e32 v41, v217
	v_mov_b32_e32 v42, v217
	v_mov_b32_e32 v43, v217
	v_mov_b32_e32 v44, v217
	v_mov_b32_e32 v45, v217
	v_mov_b32_e32 v46, v217
	v_mov_b32_e32 v47, v217
	v_mov_b32_e32 v48, v217
	v_mov_b32_e32 v49, v217
	v_mov_b32_e32 v18, 0
	v_mov_b32_e32 v19, v217
	v_mov_b32_e32 v20, v217
	v_mov_b32_e32 v21, v217
	v_mov_b32_e32 v22, v217
	v_mov_b32_e32 v23, v217
	v_mov_b32_e32 v24, v217
	v_mov_b32_e32 v25, v217
	v_mov_b32_e32 v26, v217
	v_mov_b32_e32 v27, v217
	v_mov_b32_e32 v28, v217
	v_mov_b32_e32 v29, v217
	v_mov_b32_e32 v30, v217
	v_mov_b32_e32 v31, v217
	v_mov_b32_e32 v32, v217
	v_mov_b32_e32 v33, v217

.LBB0_885:
	s_add_i32 s0, s30, 1
	ds_read_b64 v[138:139], v234 offset:256
	ds_read_b64_tr_b16 v[126:127], v221 offset:0
	ds_read_b64_tr_b16 v[128:129], v221 offset:0x800
	ds_read_b64_tr_b16 v[134:135], v221 offset:0x1000
	ds_read_b64_tr_b16 v[136:137], v221 offset:0x1800
	s_waitcnt lgkmcnt(0)
	v_lshrrev_b64 v[138:139], s0, v[138:139]
	v_and_b32_e32 v2, 1, v138
	ds_read_b64_tr_b16 v[138:139], v221 offset:0x2000
	ds_read_b64_tr_b16 v[140:141], v221 offset:0x2800
	ds_read_b64_tr_b16 v[142:143], v221 offset:0x3000
	ds_read_b64_tr_b16 v[144:145], v221 offset:0x3800
	s_waitcnt lgkmcnt(0)
	v_cmp_eq_u64_e32 vcc, 0, v[2:3]
	v_mfma_f32_32x32x16_bf16 v[66:81], v[130:133], v[126:129], v[66:81]
	v_max_f32_e32 v2, v83, v83
	v_max_f32_e32 v194, v82, v82
	v_max_f32_e32 v2, v194, v2
	v_max3_f32 v2, v2, v84, v85
	v_max3_f32 v2, v2, v86, v87
	v_max3_f32 v2, v2, v88, v89
	v_max3_f32 v2, v2, v90, v91
	v_mfma_f32_32x32x16_bf16 v[66:81], v[118:121], v[134:137], v[66:81]
	v_max3_f32 v2, v2, v92, v93
	v_max3_f32 v2, v2, v94, v95
	v_max3_f32 v2, v2, v96, v97
	v_max3_f32 v2, v2, v98, v99
	ds_read_b64_tr_b16 v[182:183], v221 offset:0x200
	v_max3_f32 v2, v2, v100, v101
	ds_read_b64_tr_b16 v[184:185], v221 offset:0xa00
	v_mfma_f32_32x32x16_bf16 v[66:81], v[114:117], v[138:141], v[66:81]
	v_max3_f32 v2, v2, v102, v103
	ds_read_b64_tr_b16 v[186:187], v221 offset:0x1200
	v_max3_f32 v2, v2, v104, v105
	ds_read_b64_tr_b16 v[188:189], v221 offset:0x1a00
	v_max3_f32 v2, v2, v106, v107
	ds_read_b64_tr_b16 v[190:191], v221 offset:0x2200
	v_max3_f32 v2, v2, v108, v109
	v_mfma_f32_32x32x16_bf16 v[66:81], v[122:125], v[142:145], v[66:81]
	ds_read_b64_tr_b16 v[192:193], v221 offset:0x2a00
	v_max3_f32 v2, v2, v110, v111
	ds_read_b64_tr_b16 v[126:127], v221 offset:0x3200
	v_max3_f32 v2, v2, v112, v113
	ds_read_b64_tr_b16 v[128:129], v221 offset:0x3a00
	v_mov_b32_e32 v134, v2
	s_nop 1
	v_permlane32_swap_b32_e32 v2, v134
	s_waitcnt lgkmcnt(0)
	v_max_f32_e32 v134, v134, v134
	v_max_f32_e32 v2, v2, v2
	v_max_f32_e32 v2, v2, v134
	v_cndmask_b32_e32 v2, v2, v228, vcc
	v_mfma_f32_32x32x16_bf16 v[50:65], v[130:133], v[182:185], v[50:65]
	v_sub_f32_e32 v194, v2, v236
	v_mul_f32_e32 v194, 0x3db504f3, v194
	v_cmp_ge_f32_e64 s[0:1], s48, v194
	s_cmp_eq_u64 s[0:1], exec
	v_max_f32_e32 v194, v236, v236
	ds_read_b64_tr_b16 v[134:135], v221 offset:0x400
	v_max_f32_e32 v2, v194, v2
	v_mfma_f32_32x32x16_bf16 v[50:65], v[118:121], v[186:189], v[50:65]
	s_cselect_b64 s[0:1], -1, 0
	ds_read_b64_tr_b16 v[136:137], v221 offset:0xc00
	v_cndmask_b32_e64 v205, v2, v236, s[0:1]
	ds_read_b64_tr_b16 v[138:139], v221 offset:0x1400
	v_sub_f32_e32 v2, v236, v205
	ds_read_b64_tr_b16 v[140:141], v221 offset:0x1c00
	v_mul_f32_e32 v2, 0x3e0293ee, v2
	v_mfma_f32_32x32x16_bf16 v[50:65], v[114:117], v[190:193], v[50:65]
	ds_read_b64_tr_b16 v[142:143], v221 offset:0x2400
	v_exp_f32_e32 v204, v2
	v_mul_f32_e32 v2, 0xbe0293ee, v205
	ds_read_b64_tr_b16 v[144:145], v221 offset:0x2c00
	v_cndmask_b32_e32 v2, v2, v228, vcc
	ds_read_b64_tr_b16 v[182:183], v221 offset:0x3400
	v_fma_f32 v96, v96, s12, v2
	v_fma_f32 v97, v97, s12, v2
	v_mfma_f32_32x32x16_bf16 v[50:65], v[122:125], v[126:129], v[50:65]
	v_fma_f32 v94, v94, s12, v2
	v_fma_f32 v95, v95, s12, v2
	v_fma_f32 v92, v92, s12, v2
	v_fma_f32 v93, v93, s12, v2
	v_fma_f32 v90, v90, s12, v2
	v_fma_f32 v91, v91, s12, v2
	v_fma_f32 v88, v88, s12, v2
	v_fma_f32 v89, v89, s12, v2
	v_fma_f32 v86, v86, s12, v2
	v_fma_f32 v87, v87, s12, v2
	v_fma_f32 v84, v84, s12, v2
	v_fma_f32 v85, v85, s12, v2
	v_fma_f32 v82, v82, s12, v2
	v_fma_f32 v83, v83, s12, v2
	v_fma_f32 v112, v112, s12, v2
	v_fma_f32 v113, v113, s12, v2
	v_fma_f32 v110, v110, s12, v2
	v_fma_f32 v111, v111, s12, v2
	v_fma_f32 v108, v108, s12, v2
	v_fma_f32 v109, v109, s12, v2
	v_fma_f32 v106, v106, s12, v2
	v_fma_f32 v107, v107, s12, v2
	v_fma_f32 v104, v104, s12, v2
	v_fma_f32 v105, v105, s12, v2
	v_fma_f32 v102, v102, s12, v2
	v_fma_f32 v103, v103, s12, v2
	v_fma_f32 v100, v100, s12, v2
	v_fma_f32 v101, v101, s12, v2
	v_fma_f32 v98, v98, s12, v2
	v_fma_f32 v99, v99, s12, v2
	ds_read_b64_tr_b16 v[184:185], v221 offset:0x3c00
	s_nop 0
	s_waitcnt lgkmcnt(0)
	v_mfma_f32_32x32x16_bf16 v[34:49], v[130:133], v[134:137], v[34:49]
	ds_read_b64_tr_b16 v[126:127], v221 offset:0x600
	ds_read_b64_tr_b16 v[128:129], v221 offset:0xe00
	ds_read_b64_tr_b16 v[134:135], v221 offset:0x1600
	ds_read_b64_tr_b16 v[136:137], v221 offset:0x1e00
	v_exp_f32_e32 v82, v82
	v_exp_f32_e32 v83, v83
	v_exp_f32_e32 v84, v84
	v_mfma_f32_32x32x16_bf16 v[34:49], v[118:121], v[138:141], v[34:49]
	ds_read_b64_tr_b16 v[138:139], v221 offset:0x2600
	ds_read_b64_tr_b16 v[140:141], v221 offset:0x2e00
	v_exp_f32_e32 v85, v85
	v_exp_f32_e32 v86, v86
	v_exp_f32_e32 v87, v87
	v_exp_f32_e32 v88, v88
	v_exp_f32_e32 v89, v89
	v_mfma_f32_32x32x16_bf16 v[34:49], v[114:117], v[142:145], v[34:49]
	ds_read_b64_tr_b16 v[142:143], v221 offset:0x3600
	ds_read_b64_tr_b16 v[144:145], v221 offset:0x3e00
	s_waitcnt lgkmcnt(0)
	v_mfma_f32_32x32x16_bf16 v[34:49], v[122:125], v[182:185], v[34:49]
	v_mfma_f32_32x32x16_bf16 v[18:33], v[130:133], v[126:129], v[18:33]
	v_exp_f32_e32 v90, v90
	v_exp_f32_e32 v91, v91
	v_exp_f32_e32 v92, v92
	v_exp_f32_e32 v93, v93
	v_exp_f32_e32 v94, v94
	v_exp_f32_e32 v95, v95
	v_exp_f32_e32 v96, v96
	v_mfma_f32_32x32x16_bf16 v[18:33], v[118:121], v[134:137], v[18:33]
	v_exp_f32_e32 v97, v97
	s_waitcnt vmcnt(2)
	s_waitcnt vmcnt(3)
	ds_write_b128 v229, v[12:15] offset:32768
	s_waitcnt vmcnt(2)
	ds_write_b128 v229, v[178:181] offset:40960
	s_waitcnt lgkmcnt(0)
	s_barrier
	v_mfma_f32_32x32x16_bf16 v[18:33], v[114:117], v[138:141], v[18:33]
	s_waitcnt vmcnt(0)
	v_cmp_gt_f32_e32 vcc, 1.0, v204
	s_waitcnt vmcnt(1)
	ds_write_b128 v227, v[4:7]
	s_waitcnt vmcnt(0)
	ds_write_b128 v227, v[8:11] offset:8192
	v_mfma_f32_32x32x16_bf16 v[18:33], v[122:125], v[142:145], v[18:33]
	s_cbranch_vccz .LBB0_889
	s_and_saveexec_b64 s[0:1], s[8:9]
	v_add_u32_e32 v2, v234, v225
	ds_write_b32 v2, v204 offset:128
	s_or_b64 exec, exec, s[0:1]
	s_waitcnt lgkmcnt(0)
	ds_read_b128 v[114:117], v232 offset:224
	ds_read_b128 v[118:121], v232 offset:192
	ds_read_b128 v[122:125], v232 offset:160
	ds_read_b128 v[126:129], v232 offset:128
	s_waitcnt lgkmcnt(3)
	v_pk_mul_f32 v[80:81], v[80:81], v[116:117]
	s_waitcnt lgkmcnt(2)
	v_pk_mul_f32 v[76:77], v[76:77], v[120:121]
	s_waitcnt lgkmcnt(1)
	v_pk_mul_f32 v[72:73], v[72:73], v[124:125]
	s_waitcnt lgkmcnt(0)
	v_pk_mul_f32 v[68:69], v[68:69], v[128:129]
	v_pk_mul_f32 v[78:79], v[78:79], v[114:115]
	v_pk_mul_f32 v[74:75], v[74:75], v[118:119]
	v_pk_mul_f32 v[70:71], v[70:71], v[122:123]
	v_pk_mul_f32 v[66:67], v[66:67], v[126:127]
	v_pk_mul_f32 v[64:65], v[64:65], v[116:117]
	v_pk_mul_f32 v[60:61], v[60:61], v[120:121]
	v_pk_mul_f32 v[56:57], v[56:57], v[124:125]
	v_pk_mul_f32 v[52:53], v[52:53], v[128:129]
	v_pk_mul_f32 v[62:63], v[62:63], v[114:115]
	v_pk_mul_f32 v[58:59], v[58:59], v[118:119]
	v_pk_mul_f32 v[54:55], v[54:55], v[122:123]
	v_pk_mul_f32 v[50:51], v[50:51], v[126:127]
	v_pk_mul_f32 v[48:49], v[48:49], v[116:117]
	v_pk_mul_f32 v[44:45], v[44:45], v[120:121]
	v_pk_mul_f32 v[40:41], v[40:41], v[124:125]
	v_pk_mul_f32 v[36:37], v[36:37], v[128:129]
	v_pk_mul_f32 v[46:47], v[46:47], v[114:115]
	v_pk_mul_f32 v[42:43], v[42:43], v[118:119]
	v_pk_mul_f32 v[38:39], v[38:39], v[122:123]
	v_pk_mul_f32 v[34:35], v[34:35], v[126:127]
	v_pk_mul_f32 v[32:33], v[32:33], v[116:117]
	v_pk_mul_f32 v[28:29], v[28:29], v[120:121]
	v_pk_mul_f32 v[24:25], v[24:25], v[124:125]
	v_pk_mul_f32 v[20:21], v[20:21], v[128:129]
	v_pk_mul_f32 v[30:31], v[30:31], v[114:115]
	v_pk_mul_f32 v[26:27], v[26:27], v[118:119]
	v_pk_mul_f32 v[22:23], v[22:23], v[122:123]
	v_pk_mul_f32 v[18:19], v[18:19], v[126:127]

.LBB0_893:
	ds_read_b64 v[212:213], v234 offset:256
	ds_read_b64_tr_b16 v[208:209], v221 offset:0x4000
	ds_read_b64_tr_b16 v[210:211], v221 offset:0x4800
	ds_read_b64_tr_b16 v[236:237], v221 offset:0x5000
	ds_read_b64_tr_b16 v[238:239], v221 offset:0x5800
	ds_read_b64_tr_b16 v[240:241], v221 offset:0x6000
	ds_read_b64_tr_b16 v[242:243], v221 offset:0x6800
	ds_read_b64_tr_b16 v[244:245], v221 offset:0x7000
	ds_read_b64_tr_b16 v[246:247], v221 offset:0x7800
	s_waitcnt lgkmcnt(0)
	s_waitcnt lgkmcnt(0)
	v_lshrrev_b64 v[212:213], s30, v[212:213]
	v_and_b32_e32 v2, 1, v212
	v_cmp_eq_u64_e32 vcc, 0, v[2:3]
	v_mfma_f32_32x32x16_bf16 v[66:81], v[190:193], v[208:211], v[66:81]
	v_max_f32_e32 v2, v115, v115
	v_max_f32_e32 v212, v114, v114
	v_max_f32_e32 v2, v212, v2
	v_max3_f32 v2, v2, v116, v117
	v_max3_f32 v2, v2, v118, v119
	v_max3_f32 v2, v2, v120, v121
	v_max3_f32 v2, v2, v122, v123
	v_mfma_f32_32x32x16_bf16 v[66:81], v[194:197], v[236:239], v[66:81]
	v_max3_f32 v2, v2, v124, v125
	v_max3_f32 v2, v2, v126, v127
	v_max3_f32 v2, v2, v128, v129
	v_max3_f32 v2, v2, v130, v131
	ds_read_b64_tr_b16 v[208:209], v221 offset:0x4200
	v_max3_f32 v2, v2, v132, v133
	ds_read_b64_tr_b16 v[210:211], v221 offset:0x4a00
	v_mfma_f32_32x32x16_bf16 v[66:81], v[186:189], v[240:243], v[66:81]
	v_max3_f32 v2, v2, v134, v135
	ds_read_b64_tr_b16 v[236:237], v221 offset:0x5200
	v_max3_f32 v2, v2, v136, v137
	ds_read_b64_tr_b16 v[238:239], v221 offset:0x5a00
	v_max3_f32 v2, v2, v138, v139
	ds_read_b64_tr_b16 v[240:241], v221 offset:0x6200
	v_max3_f32 v2, v2, v140, v141
	v_mfma_f32_32x32x16_bf16 v[66:81], v[182:185], v[244:247], v[66:81]
	ds_read_b64_tr_b16 v[242:243], v221 offset:0x6a00
	v_max3_f32 v2, v2, v142, v143
	ds_read_b64_tr_b16 v[244:245], v221 offset:0x7200
	v_max3_f32 v2, v2, v144, v145
	ds_read_b64_tr_b16 v[246:247], v221 offset:0x7a00
	v_mov_b32_e32 v212, v2
	s_nop 1
	v_permlane32_swap_b32_e32 v2, v212
	s_waitcnt lgkmcnt(0)
	v_max_f32_e32 v212, v212, v212
	v_max_f32_e32 v2, v2, v2
	v_max_f32_e32 v2, v2, v212
	v_cndmask_b32_e32 v2, v2, v228, vcc
	v_mfma_f32_32x32x16_bf16 v[50:65], v[190:193], v[208:211], v[50:65]
	v_sub_f32_e32 v212, v2, v205
	v_mul_f32_e32 v212, 0x3db504f3, v212
	ds_read_b64_tr_b16 v[208:209], v221 offset:0x4400
	v_cmp_ge_f32_e64 s[0:1], s48, v212
	ds_read_b64_tr_b16 v[210:211], v221 offset:0x4c00
	s_cmp_eq_u64 s[0:1], exec
	v_max_f32_e32 v212, v205, v205
	v_mfma_f32_32x32x16_bf16 v[50:65], v[194:197], v[236:239], v[50:65]
	ds_read_b64_tr_b16 v[238:239], v221 offset:0x5400
	s_cselect_b64 s[0:1], -1, 0
	v_max_f32_e32 v2, v212, v2
	v_cndmask_b32_e64 v236, v2, v205, s[0:1]
	v_mul_f32_e32 v2, 0xbe0293ee, v236
	v_cndmask_b32_e32 v2, v2, v228, vcc
	v_fma_f32 v128, v128, s12, v2
	v_fma_f32 v129, v129, s12, v2
	v_mfma_f32_32x32x16_bf16 v[50:65], v[186:189], v[240:243], v[50:65]
	ds_read_b64_tr_b16 v[240:241], v221 offset:0x5c00
	ds_read_b64_tr_b16 v[242:243], v221 offset:0x6400
	v_fma_f32 v126, v126, s12, v2
	v_fma_f32 v127, v127, s12, v2
	v_fma_f32 v124, v124, s12, v2
	v_fma_f32 v125, v125, s12, v2
	v_fma_f32 v122, v122, s12, v2
	v_fma_f32 v123, v123, s12, v2
	v_fma_f32 v120, v120, s12, v2
	v_fma_f32 v121, v121, s12, v2
	v_fma_f32 v118, v118, s12, v2
	v_fma_f32 v119, v119, s12, v2
	v_mfma_f32_32x32x16_bf16 v[50:65], v[182:185], v[244:247], v[50:65]
	ds_read_b64_tr_b16 v[244:245], v221 offset:0x6c00
	ds_read_b64_tr_b16 v[246:247], v221 offset:0x7400
	v_fma_f32 v116, v116, s12, v2
	v_fma_f32 v117, v117, s12, v2
	v_fma_f32 v114, v114, s12, v2
	v_fma_f32 v115, v115, s12, v2
	v_fma_f32 v144, v144, s12, v2
	v_fma_f32 v145, v145, s12, v2
	v_fma_f32 v142, v142, s12, v2
	v_fma_f32 v143, v143, s12, v2
	v_fma_f32 v140, v140, s12, v2
	v_fma_f32 v141, v141, s12, v2
	v_fma_f32 v138, v138, s12, v2
	v_fma_f32 v139, v139, s12, v2
	v_fma_f32 v136, v136, s12, v2
	v_fma_f32 v137, v137, s12, v2
	v_fma_f32 v134, v134, s12, v2
	v_fma_f32 v135, v135, s12, v2
	v_fma_f32 v132, v132, s12, v2
	v_fma_f32 v133, v133, s12, v2
	v_fma_f32 v130, v130, s12, v2
	v_fma_f32 v131, v131, s12, v2
	ds_read_b64_tr_b16 v[248:249], v221 offset:0x7c00
	s_nop 0
	s_waitcnt lgkmcnt(0)
	v_mfma_f32_32x32x16_bf16 v[34:49], v[190:193], v[208:211], v[34:49]
	ds_read_b64_tr_b16 v[208:209], v221 offset:0x4600
	ds_read_b64_tr_b16 v[210:211], v221 offset:0x4e00
	ds_read_b64_tr_b16 v[250:251], v221 offset:0x5600
	ds_read_b64_tr_b16 v[252:253], v221 offset:0x5e00
	v_exp_f32_e32 v114, v114
	v_exp_f32_e32 v115, v115
	v_exp_f32_e32 v116, v116
	v_mfma_f32_32x32x16_bf16 v[34:49], v[194:197], v[238:241], v[34:49]
	ds_read_b64_tr_b16 v[238:239], v221 offset:0x6600
	ds_read_b64_tr_b16 v[240:241], v221 offset:0x6e00
	v_exp_f32_e32 v117, v117
	v_exp_f32_e32 v118, v118
	v_exp_f32_e32 v119, v119
	v_exp_f32_e32 v120, v120
	v_exp_f32_e32 v121, v121
	v_mfma_f32_32x32x16_bf16 v[34:49], v[186:189], v[242:245], v[34:49]
	ds_read_b64_tr_b16 v[242:243], v221 offset:0x7600
	ds_read_b64_tr_b16 v[244:245], v221 offset:0x7e00
	s_waitcnt lgkmcnt(0)
	v_mfma_f32_32x32x16_bf16 v[34:49], v[182:185], v[246:249], v[34:49]
	v_mfma_f32_32x32x16_bf16 v[18:33], v[190:193], v[208:211], v[18:33]
	v_cndmask_b32_e64 v2, 0, 1, s[28:29]
	v_exp_f32_e32 v122, v122
	v_exp_f32_e32 v123, v123
	v_exp_f32_e32 v124, v124
	v_exp_f32_e32 v125, v125
	v_exp_f32_e32 v126, v126
	v_exp_f32_e32 v127, v127
	v_mfma_f32_32x32x16_bf16 v[18:33], v[194:197], v[250:253], v[18:33]
	v_exp_f32_e32 v128, v128
	v_exp_f32_e32 v129, v129
	v_cmp_ne_u32_e64 s[0:1], 1, v2
	s_andn2_b64 vcc, exec, s[28:29]
	v_mfma_f32_32x32x16_bf16 v[18:33], v[186:189], v[238:241], v[18:33]
	v_mfma_f32_32x32x16_bf16 v[18:33], v[182:185], v[242:245], v[18:33]
	s_cbranch_vccnz .LBB0_895
	s_waitcnt vmcnt(2)
	s_waitcnt vmcnt(3)
	ds_write_b128 v229, v[12:15] offset:49152
	s_waitcnt vmcnt(2)
	ds_write_b128 v229, v[178:181] offset:57344

.LBB0_1112:
	v_max_f32_e32 v36, 0xf149f2ca, v2
	v_cndmask_b32_e64 v236, v36, v231, s[0:1]
	v_mul_f32_e32 v2, 0xbe0293ee, v236
	v_fmamk_f32 v20, v20, 0x3e0293ee, v2
	v_exp_f32_e32 v114, v20
	v_sub_f32_e32 v20, 0xf149f2ca, v36
	v_mul_f32_e32 v20, 0x3e0293ee, v20
	v_fmamk_f32 v21, v21, 0x3e0293ee, v2
	v_fmamk_f32 v22, v22, 0x3e0293ee, v2
	v_fmamk_f32 v23, v23, 0x3e0293ee, v2
	v_fmamk_f32 v24, v24, 0x3e0293ee, v2
	v_fmamk_f32 v25, v25, 0x3e0293ee, v2
	v_fmamk_f32 v26, v26, 0x3e0293ee, v2
	v_fmamk_f32 v27, v27, 0x3e0293ee, v2
	v_fmamk_f32 v28, v28, 0x3e0293ee, v2
	v_fmamk_f32 v29, v29, 0x3e0293ee, v2
	v_fmamk_f32 v30, v30, 0x3e0293ee, v2
	v_fmamk_f32 v31, v31, 0x3e0293ee, v2
	v_fmamk_f32 v32, v32, 0x3e0293ee, v2
	v_fmamk_f32 v33, v33, 0x3e0293ee, v2
	v_fmamk_f32 v34, v34, 0x3e0293ee, v2
	v_fmamk_f32 v35, v35, 0x3e0293ee, v2
	v_exp_f32_e32 v20, v20
	v_exp_f32_e32 v115, v21
	v_exp_f32_e32 v116, v22
	v_exp_f32_e32 v117, v23
	v_exp_f32_e32 v118, v24
	v_exp_f32_e32 v119, v25
	v_exp_f32_e32 v120, v26
	v_exp_f32_e32 v121, v27
	v_exp_f32_e32 v122, v28
	v_exp_f32_e32 v123, v29
	v_exp_f32_e32 v124, v30
	v_exp_f32_e32 v125, v31
	v_exp_f32_e32 v126, v32
	v_exp_f32_e32 v127, v33
	v_exp_f32_e32 v128, v34
	v_exp_f32_e32 v129, v35
	v_cndmask_b32_e64 v235, v20, 1.0, s[0:1]
	v_fma_f32 v144, v18, s10, v2
	v_fma_f32 v145, v19, s10, v2
	v_fma_f32 v142, v16, s10, v2
	v_fma_f32 v143, v17, s10, v2
	v_fma_f32 v140, v14, s10, v2
	v_fma_f32 v141, v15, s10, v2
	v_fma_f32 v138, v12, s10, v2
	v_fma_f32 v139, v13, s10, v2
	v_fma_f32 v136, v10, s10, v2
	v_fma_f32 v137, v11, s10, v2
	v_fma_f32 v134, v8, s10, v2
	v_fma_f32 v135, v9, s10, v2
	v_fma_f32 v132, v6, s10, v2
	v_fma_f32 v133, v7, s10, v2
	v_fma_f32 v130, v4, s10, v2
	v_fma_f32 v131, v5, s10, v2
	s_cmp_lt_i32 s57, 3
	v_lshl_add_u32 v233, v227, 2, s59
	s_waitcnt lgkmcnt(0)
	s_barrier
	s_cbranch_scc1 .LBB0_1133
	v_mov_b32_e32 v217, v3
	s_add_i32 s0, s55, s58
	v_add_u32_e32 v2, 0xffffff45, v220
	v_lshl_add_u64 v[16:17], s[24:25], 0, v[216:217]
	v_lshl_add_u64 v[198:199], s[26:27], 0, v[216:217]
	v_add_u32_e32 v2, s0, v2
	s_lshl_b32 s0, s60, 15
	v_mov_b32_e32 v217, 0
	s_mov_b32 s26, 2
	v_subrev_u32_e32 v2, s4, v2
	s_add_i32 s27, s4, 0xbf
	s_add_i32 s4, s0, 0x10000
	v_mov_b32_e32 v66, 0
	v_mov_b32_e32 v67, v217
	v_mov_b32_e32 v68, v217
	v_mov_b32_e32 v69, v217
	v_mov_b32_e32 v70, v217
	v_mov_b32_e32 v71, v217
	v_mov_b32_e32 v72, v217
	v_mov_b32_e32 v73, v217
	v_mov_b32_e32 v74, v217
	v_mov_b32_e32 v75, v217
	v_mov_b32_e32 v76, v217
	v_mov_b32_e32 v77, v217
	v_mov_b32_e32 v78, v217
	v_mov_b32_e32 v79, v217
	v_mov_b32_e32 v80, v217
	v_mov_b32_e32 v81, v217
	v_mov_b32_e32 v50, 0
	v_mov_b32_e32 v51, v217
	v_mov_b32_e32 v52, v217
	v_mov_b32_e32 v53, v217
	v_mov_b32_e32 v54, v217
	v_mov_b32_e32 v55, v217
	v_mov_b32_e32 v56, v217
	v_mov_b32_e32 v57, v217
	v_mov_b32_e32 v58, v217
	v_mov_b32_e32 v59, v217
	v_mov_b32_e32 v60, v217
	v_mov_b32_e32 v61, v217
	v_mov_b32_e32 v62, v217
	v_mov_b32_e32 v63, v217
	v_mov_b32_e32 v64, v217
	v_mov_b32_e32 v65, v217
	v_mov_b32_e32 v34, 0
	v_mov_b32_e32 v35, v217
	v_mov_b32_e32 v36, v217
	v_mov_b32_e32 v37, v217
	v_mov_b32_e32 v38, v217
	v_mov_b32_e32 v39, v217
	v_mov_b32_e32 v40, v217
	v_mov_b32_e32 v41, v217
	v_mov_b32_e32 v42, v217
	v_mov_b32_e32 v43, v217
	v_mov_b32_e32 v44, v217
	v_mov_b32_e32 v45, v217
	v_mov_b32_e32 v46, v217
	v_mov_b32_e32 v47, v217
	v_mov_b32_e32 v48, v217
	v_mov_b32_e32 v49, v217
	v_mov_b32_e32 v18, 0
	v_mov_b32_e32 v19, v217
	v_mov_b32_e32 v20, v217
	v_mov_b32_e32 v21, v217
	v_mov_b32_e32 v22, v217
	v_mov_b32_e32 v23, v217
	v_mov_b32_e32 v24, v217
	v_mov_b32_e32 v25, v217
	v_mov_b32_e32 v26, v217
	v_mov_b32_e32 v27, v217
	v_mov_b32_e32 v28, v217
	v_mov_b32_e32 v29, v217
	v_mov_b32_e32 v30, v217
	v_mov_b32_e32 v31, v217
	v_mov_b32_e32 v32, v217
	v_mov_b32_e32 v33, v217
	s_branch .LBB0_1116

.LBB0_1118:
	ds_read_b64_tr_b16 v[126:127], v221 offset:0
	ds_read_b64_tr_b16 v[128:129], v221 offset:0x800
	ds_read_b64_tr_b16 v[134:135], v221 offset:0x1000
	ds_read_b64_tr_b16 v[136:137], v221 offset:0x1800
	ds_read_b64_tr_b16 v[138:139], v221 offset:0x2000
	ds_read_b64_tr_b16 v[140:141], v221 offset:0x2800
	ds_read_b64_tr_b16 v[142:143], v221 offset:0x3000
	ds_read_b64_tr_b16 v[144:145], v221 offset:0x3800
	s_waitcnt lgkmcnt(0)
	s_nop 0
	v_mfma_f32_32x32x16_bf16 v[66:81], v[130:133], v[126:129], v[66:81]
	v_max_f32_e32 v194, v83, v83
	v_max_f32_e32 v195, v82, v82
	v_max_f32_e32 v194, v195, v194
	v_max3_f32 v194, v194, v84, v85
	v_max3_f32 v194, v194, v86, v87
	ds_read_b64_tr_b16 v[182:183], v221 offset:0x200
	ds_read_b64_tr_b16 v[184:185], v221 offset:0xa00
	v_mfma_f32_32x32x16_bf16 v[66:81], v[118:121], v[134:137], v[66:81]
	v_max3_f32 v134, v194, v88, v89
	v_max3_f32 v134, v134, v90, v91
	v_max3_f32 v134, v134, v92, v93
	v_max3_f32 v134, v134, v94, v95
	v_max3_f32 v134, v134, v96, v97
	v_max3_f32 v134, v134, v98, v99
	v_max3_f32 v134, v134, v100, v101
	v_mfma_f32_32x32x16_bf16 v[66:81], v[114:117], v[138:141], v[66:81]
	ds_read_b64_tr_b16 v[186:187], v221 offset:0x1200
	v_max3_f32 v134, v134, v102, v103
	ds_read_b64_tr_b16 v[188:189], v221 offset:0x1a00
	v_max3_f32 v134, v134, v104, v105
	ds_read_b64_tr_b16 v[190:191], v221 offset:0x2200
	v_max3_f32 v134, v134, v106, v107
	ds_read_b64_tr_b16 v[192:193], v221 offset:0x2a00
	v_mfma_f32_32x32x16_bf16 v[66:81], v[122:125], v[142:145], v[66:81]
	v_max3_f32 v134, v134, v108, v109
	ds_read_b64_tr_b16 v[126:127], v221 offset:0x3200
	v_max3_f32 v134, v134, v110, v111
	ds_read_b64_tr_b16 v[128:129], v221 offset:0x3a00
	v_max3_f32 v134, v134, v112, v113
	v_mov_b32_e32 v135, v134
	s_waitcnt lgkmcnt(0)
	s_nop 1
	v_permlane32_swap_b32_e32 v134, v135
	v_max_f32_e32 v135, v135, v135
	v_max_f32_e32 v134, v134, v134
	v_max_f32_e32 v194, v134, v135
	v_mfma_f32_32x32x16_bf16 v[50:65], v[130:133], v[182:185], v[50:65]
	v_sub_f32_e32 v195, v194, v236
	v_mul_f32_e32 v195, 0x3db504f3, v195
	v_cmp_ge_f32_e32 vcc, s43, v195
	ds_read_b64_tr_b16 v[134:135], v221 offset:0x400
	s_cmp_eq_u64 vcc, exec
	v_max_f32_e32 v195, v236, v236
	ds_read_b64_tr_b16 v[136:137], v221 offset:0xc00
	v_mfma_f32_32x32x16_bf16 v[50:65], v[118:121], v[186:189], v[50:65]
	v_max_f32_e32 v186, v195, v194
	s_cselect_b64 vcc, -1, 0
	ds_read_b64_tr_b16 v[138:139], v221 offset:0x1400
	v_cndmask_b32_e32 v208, v186, v236, vcc
	ds_read_b64_tr_b16 v[140:141], v221 offset:0x1c00
	v_sub_f32_e32 v186, v236, v208
	ds_read_b64_tr_b16 v[142:143], v221 offset:0x2400
	v_mfma_f32_32x32x16_bf16 v[50:65], v[114:117], v[190:193], v[50:65]
	v_mul_f32_e32 v186, 0x3e0293ee, v186
	ds_read_b64_tr_b16 v[144:145], v221 offset:0x2c00
	v_exp_f32_e32 v207, v186
	v_mul_f32_e32 v186, 0xbe0293ee, v208
	ds_read_b64_tr_b16 v[182:183], v221 offset:0x3400
	v_fma_f32 v96, v96, s10, v186
	v_fma_f32 v97, v97, s10, v186
	v_fma_f32 v94, v94, s10, v186
	v_fma_f32 v95, v95, s10, v186
	v_mfma_f32_32x32x16_bf16 v[50:65], v[122:125], v[126:129], v[50:65]
	v_fma_f32 v92, v92, s10, v186
	v_fma_f32 v93, v93, s10, v186
	v_fma_f32 v90, v90, s10, v186
	v_fma_f32 v91, v91, s10, v186
	v_fma_f32 v88, v88, s10, v186
	v_fma_f32 v89, v89, s10, v186
	v_fma_f32 v86, v86, s10, v186
	v_fma_f32 v87, v87, s10, v186
	v_fma_f32 v84, v84, s10, v186
	v_fma_f32 v85, v85, s10, v186
	v_fma_f32 v82, v82, s10, v186
	v_fma_f32 v83, v83, s10, v186
	v_fma_f32 v112, v112, s10, v186
	v_fma_f32 v113, v113, s10, v186
	v_fma_f32 v110, v110, s10, v186
	v_fma_f32 v111, v111, s10, v186
	v_fma_f32 v108, v108, s10, v186
	v_fma_f32 v109, v109, s10, v186
	v_fma_f32 v106, v106, s10, v186
	v_fma_f32 v107, v107, s10, v186
	v_fma_f32 v104, v104, s10, v186
	v_fma_f32 v105, v105, s10, v186
	v_fma_f32 v102, v102, s10, v186
	v_fma_f32 v103, v103, s10, v186
	v_fma_f32 v100, v100, s10, v186
	v_fma_f32 v101, v101, s10, v186
	v_fma_f32 v98, v98, s10, v186
	v_fma_f32 v99, v99, s10, v186
	ds_read_b64_tr_b16 v[184:185], v221 offset:0x3c00
	s_nop 0
	s_waitcnt lgkmcnt(0)
	v_mfma_f32_32x32x16_bf16 v[34:49], v[130:133], v[134:137], v[34:49]
	ds_read_b64_tr_b16 v[126:127], v221 offset:0x600
	ds_read_b64_tr_b16 v[128:129], v221 offset:0xe00
	ds_read_b64_tr_b16 v[134:135], v221 offset:0x1600
	ds_read_b64_tr_b16 v[136:137], v221 offset:0x1e00
	v_exp_f32_e32 v82, v82
	v_exp_f32_e32 v83, v83
	v_exp_f32_e32 v84, v84
	v_mfma_f32_32x32x16_bf16 v[34:49], v[118:121], v[138:141], v[34:49]
	ds_read_b64_tr_b16 v[138:139], v221 offset:0x2600
	ds_read_b64_tr_b16 v[140:141], v221 offset:0x2e00
	v_exp_f32_e32 v85, v85
	v_exp_f32_e32 v86, v86
	v_exp_f32_e32 v87, v87
	v_exp_f32_e32 v88, v88
	v_exp_f32_e32 v89, v89
	v_mfma_f32_32x32x16_bf16 v[34:49], v[114:117], v[142:145], v[34:49]
	ds_read_b64_tr_b16 v[142:143], v221 offset:0x3600
	ds_read_b64_tr_b16 v[144:145], v221 offset:0x3e00
	s_waitcnt lgkmcnt(0)
	v_mfma_f32_32x32x16_bf16 v[34:49], v[122:125], v[182:185], v[34:49]
	v_mfma_f32_32x32x16_bf16 v[18:33], v[130:133], v[126:129], v[18:33]
	v_exp_f32_e32 v90, v90
	v_exp_f32_e32 v91, v91
	v_exp_f32_e32 v92, v92
	v_exp_f32_e32 v93, v93
	v_exp_f32_e32 v94, v94
	v_exp_f32_e32 v95, v95
	v_exp_f32_e32 v96, v96
	v_mfma_f32_32x32x16_bf16 v[18:33], v[118:121], v[134:137], v[18:33]
	v_exp_f32_e32 v97, v97
	s_waitcnt vmcnt(2)
	s_waitcnt vmcnt(3)
	ds_write_b128 v230, v[12:15] offset:32768
	s_waitcnt vmcnt(2)
	ds_write_b128 v230, v[178:181] offset:40960
	s_waitcnt lgkmcnt(0)
	s_barrier
	v_mfma_f32_32x32x16_bf16 v[18:33], v[114:117], v[138:141], v[18:33]
	s_waitcnt vmcnt(0)
	v_cmp_gt_f32_e32 vcc, 1.0, v207
	s_waitcnt vmcnt(1)
	ds_write_b128 v228, v[4:7]
	s_waitcnt vmcnt(0)
	ds_write_b128 v228, v[8:11] offset:8192
	v_mfma_f32_32x32x16_bf16 v[18:33], v[122:125], v[142:145], v[18:33]
	s_cbranch_vccz .LBB0_1122
	s_and_saveexec_b64 s[0:1], s[8:9]
	ds_write_b32 v232, v207 offset:128
	s_or_b64 exec, exec, s[0:1]
	s_waitcnt lgkmcnt(0)
	ds_read_b128 v[114:117], v233 offset:224
	ds_read_b128 v[118:121], v233 offset:192
	ds_read_b128 v[122:125], v233 offset:160
	ds_read_b128 v[126:129], v233 offset:128
	s_waitcnt lgkmcnt(3)
	v_pk_mul_f32 v[80:81], v[80:81], v[116:117]
	s_waitcnt lgkmcnt(2)
	v_pk_mul_f32 v[76:77], v[76:77], v[120:121]
	s_waitcnt lgkmcnt(1)
	v_pk_mul_f32 v[72:73], v[72:73], v[124:125]
	s_waitcnt lgkmcnt(0)
	v_pk_mul_f32 v[68:69], v[68:69], v[128:129]
	v_pk_mul_f32 v[78:79], v[78:79], v[114:115]
	v_pk_mul_f32 v[74:75], v[74:75], v[118:119]
	v_pk_mul_f32 v[70:71], v[70:71], v[122:123]
	v_pk_mul_f32 v[66:67], v[66:67], v[126:127]
	v_pk_mul_f32 v[64:65], v[64:65], v[116:117]
	v_pk_mul_f32 v[60:61], v[60:61], v[120:121]
	v_pk_mul_f32 v[56:57], v[56:57], v[124:125]
	v_pk_mul_f32 v[52:53], v[52:53], v[128:129]
	v_pk_mul_f32 v[62:63], v[62:63], v[114:115]
	v_pk_mul_f32 v[58:59], v[58:59], v[118:119]
	v_pk_mul_f32 v[54:55], v[54:55], v[122:123]
	v_pk_mul_f32 v[50:51], v[50:51], v[126:127]
	v_pk_mul_f32 v[48:49], v[48:49], v[116:117]
	v_pk_mul_f32 v[44:45], v[44:45], v[120:121]
	v_pk_mul_f32 v[40:41], v[40:41], v[124:125]
	v_pk_mul_f32 v[36:37], v[36:37], v[128:129]
	v_pk_mul_f32 v[46:47], v[46:47], v[114:115]
	v_pk_mul_f32 v[42:43], v[42:43], v[118:119]
	v_pk_mul_f32 v[38:39], v[38:39], v[122:123]
	v_pk_mul_f32 v[34:35], v[34:35], v[126:127]
	v_pk_mul_f32 v[32:33], v[32:33], v[116:117]
	v_pk_mul_f32 v[28:29], v[28:29], v[120:121]
	v_pk_mul_f32 v[24:25], v[24:25], v[124:125]
	v_pk_mul_f32 v[20:21], v[20:21], v[128:129]
	v_pk_mul_f32 v[30:31], v[30:31], v[114:115]
	v_pk_mul_f32 v[26:27], v[26:27], v[118:119]
	v_pk_mul_f32 v[22:23], v[22:23], v[122:123]
	v_pk_mul_f32 v[18:19], v[18:19], v[126:127]

.LBB0_1126:
	ds_read_b64_tr_b16 v[236:237], v221 offset:0x4000
	ds_read_b64_tr_b16 v[238:239], v221 offset:0x4800
	ds_read_b64_tr_b16 v[240:241], v221 offset:0x5000
	ds_read_b64_tr_b16 v[242:243], v221 offset:0x5800
	ds_read_b64_tr_b16 v[244:245], v221 offset:0x6000
	ds_read_b64_tr_b16 v[246:247], v221 offset:0x6800
	ds_read_b64_tr_b16 v[248:249], v221 offset:0x7000
	ds_read_b64_tr_b16 v[250:251], v221 offset:0x7800
	s_waitcnt lgkmcnt(0)
	s_nop 0
	v_mfma_f32_32x32x16_bf16 v[66:81], v[190:193], v[236:239], v[66:81]
	v_max_f32_e32 v211, v115, v115
	v_max_f32_e32 v212, v114, v114
	v_max_f32_e32 v211, v212, v211
	v_max3_f32 v211, v211, v116, v117
	v_max3_f32 v211, v211, v118, v119
	v_max3_f32 v211, v211, v120, v121
	v_max3_f32 v211, v211, v122, v123
	v_mfma_f32_32x32x16_bf16 v[66:81], v[194:197], v[240:243], v[66:81]
	v_max3_f32 v211, v211, v124, v125
	v_max3_f32 v211, v211, v126, v127
	v_max3_f32 v211, v211, v128, v129
	ds_read_b64_tr_b16 v[236:237], v221 offset:0x4200
	v_max3_f32 v211, v211, v130, v131
	ds_read_b64_tr_b16 v[238:239], v221 offset:0x4a00
	v_max3_f32 v211, v211, v132, v133
	v_mfma_f32_32x32x16_bf16 v[66:81], v[186:189], v[244:247], v[66:81]
	ds_read_b64_tr_b16 v[240:241], v221 offset:0x5200
	v_max3_f32 v211, v211, v134, v135
	ds_read_b64_tr_b16 v[242:243], v221 offset:0x5a00
	v_max3_f32 v211, v211, v136, v137
	ds_read_b64_tr_b16 v[244:245], v221 offset:0x6200
	v_max3_f32 v211, v211, v138, v139
	ds_read_b64_tr_b16 v[246:247], v221 offset:0x6a00
	v_mfma_f32_32x32x16_bf16 v[66:81], v[182:185], v[248:251], v[66:81]
	v_max3_f32 v211, v211, v140, v141
	ds_read_b64_tr_b16 v[248:249], v221 offset:0x7200
	v_max3_f32 v211, v211, v142, v143
	ds_read_b64_tr_b16 v[250:251], v221 offset:0x7a00
	v_max3_f32 v211, v211, v144, v145
	v_mov_b32_e32 v212, v211
	s_waitcnt lgkmcnt(0)
	s_nop 1
	v_permlane32_swap_b32_e32 v211, v212
	v_max_f32_e32 v212, v212, v212
	v_max_f32_e32 v211, v211, v211
	v_max_f32_e32 v211, v211, v212
	v_mfma_f32_32x32x16_bf16 v[50:65], v[190:193], v[236:239], v[50:65]
	v_sub_f32_e32 v212, v211, v208
	ds_read_b64_tr_b16 v[238:239], v221 offset:0x4400
	v_mul_f32_e32 v212, 0x3db504f3, v212
	v_cmp_ge_f32_e32 vcc, s43, v212
	s_cmp_eq_u64 vcc, exec
	v_max_f32_e32 v212, v208, v208
	s_cselect_b64 vcc, -1, 0
	v_mfma_f32_32x32x16_bf16 v[50:65], v[194:197], v[240:243], v[50:65]
	ds_read_b64_tr_b16 v[240:241], v221 offset:0x4c00
	ds_read_b64_tr_b16 v[242:243], v221 offset:0x5400
	v_max_f32_e32 v211, v212, v211
	v_cndmask_b32_e32 v236, v211, v208, vcc
	v_mul_f32_e32 v212, 0xbe0293ee, v236
	v_fma_f32 v128, v128, s10, v212
	v_fma_f32 v129, v129, s10, v212
	v_fma_f32 v126, v126, s10, v212
	v_fma_f32 v127, v127, s10, v212
	v_mfma_f32_32x32x16_bf16 v[50:65], v[186:189], v[244:247], v[50:65]
	ds_read_b64_tr_b16 v[244:245], v221 offset:0x5c00
	ds_read_b64_tr_b16 v[246:247], v221 offset:0x6400
	v_fma_f32 v124, v124, s10, v212
	v_fma_f32 v125, v125, s10, v212
	v_fma_f32 v122, v122, s10, v212
	v_fma_f32 v123, v123, s10, v212
	v_fma_f32 v120, v120, s10, v212
	v_fma_f32 v121, v121, s10, v212
	v_fma_f32 v118, v118, s10, v212
	v_fma_f32 v119, v119, s10, v212
	v_fma_f32 v116, v116, s10, v212
	v_fma_f32 v117, v117, s10, v212
	v_mfma_f32_32x32x16_bf16 v[50:65], v[182:185], v[248:251], v[50:65]
	ds_read_b64_tr_b16 v[248:249], v221 offset:0x6c00
	ds_read_b64_tr_b16 v[250:251], v221 offset:0x7400
	v_fma_f32 v114, v114, s10, v212
	v_fma_f32 v115, v115, s10, v212
	v_fma_f32 v144, v144, s10, v212
	v_fma_f32 v145, v145, s10, v212
	v_fma_f32 v142, v142, s10, v212
	v_fma_f32 v143, v143, s10, v212
	v_fma_f32 v140, v140, s10, v212
	v_fma_f32 v141, v141, s10, v212
	v_fma_f32 v138, v138, s10, v212
	v_fma_f32 v139, v139, s10, v212
	v_fma_f32 v136, v136, s10, v212
	v_fma_f32 v137, v137, s10, v212
	v_fma_f32 v134, v134, s10, v212
	v_fma_f32 v135, v135, s10, v212
	v_fma_f32 v132, v132, s10, v212
	v_fma_f32 v133, v133, s10, v212
	v_fma_f32 v130, v130, s10, v212
	v_fma_f32 v131, v131, s10, v212
	ds_read_b64_tr_b16 v[252:253], v221 offset:0x7c00
	s_nop 0
	s_waitcnt lgkmcnt(0)
	v_mfma_f32_32x32x16_bf16 v[34:49], v[190:193], v[238:241], v[34:49]
	ds_read_b64_tr_b16 v[238:239], v221 offset:0x4600
	ds_read_b64_tr_b16 v[240:241], v221 offset:0x4e00
	ds_read_b64_tr_b16 v[212:213], v221 offset:0x5600
	ds_read_b64_tr_b16 v[214:215], v221 offset:0x5e00
	v_exp_f32_e32 v114, v114
	v_exp_f32_e32 v115, v115
	v_exp_f32_e32 v116, v116
	v_mfma_f32_32x32x16_bf16 v[34:49], v[194:197], v[242:245], v[34:49]
	ds_read_b64_tr_b16 v[242:243], v221 offset:0x6600
	ds_read_b64_tr_b16 v[244:245], v221 offset:0x6e00
	v_exp_f32_e32 v117, v117
	v_exp_f32_e32 v118, v118
	v_exp_f32_e32 v119, v119
	v_exp_f32_e32 v120, v120
	v_exp_f32_e32 v121, v121
	v_mfma_f32_32x32x16_bf16 v[34:49], v[186:189], v[246:249], v[34:49]
	ds_read_b64_tr_b16 v[246:247], v221 offset:0x7600
	ds_read_b64_tr_b16 v[248:249], v221 offset:0x7e00
	s_waitcnt lgkmcnt(0)
	v_mfma_f32_32x32x16_bf16 v[34:49], v[182:185], v[250:253], v[34:49]
	v_mfma_f32_32x32x16_bf16 v[18:33], v[190:193], v[238:241], v[18:33]
	v_exp_f32_e32 v122, v122
	v_exp_f32_e32 v123, v123
	v_exp_f32_e32 v124, v124
	v_exp_f32_e32 v125, v125
	v_exp_f32_e32 v126, v126
	v_exp_f32_e32 v127, v127
	v_exp_f32_e32 v128, v128
	v_mfma_f32_32x32x16_bf16 v[18:33], v[194:197], v[212:215], v[18:33]
	v_exp_f32_e32 v129, v129
	s_andn2_b64 vcc, exec, s[24:25]
	v_mfma_f32_32x32x16_bf16 v[18:33], v[186:189], v[242:245], v[18:33]
	v_cndmask_b32_e64 v186, 0, 1, s[24:25]
	v_cmp_ne_u32_e64 s[0:1], 1, v186
	v_mfma_f32_32x32x16_bf16 v[18:33], v[182:185], v[246:249], v[18:33]
	s_cbranch_vccnz .LBB0_1128
	s_waitcnt vmcnt(2)
	s_waitcnt vmcnt(3)
	ds_write_b128 v230, v[12:15] offset:49152
	s_waitcnt vmcnt(2)
	ds_write_b128 v230, v[178:181] offset:57344

.LBB0_1866:
	v_max_f32_e32 v35, 0xf149f2ca, v34
	v_cndmask_b32_e64 v215, v35, v209, s[0:1]
	v_mul_f32_e32 v34, 0xbe0293ee, v215
	v_fmamk_f32 v18, v18, 0x3e0293ee, v34
	v_exp_f32_e32 v98, v18
	v_sub_f32_e32 v18, 0xf149f2ca, v35
	v_mul_f32_e32 v18, 0x3e0293ee, v18
	v_exp_f32_e32 v18, v18
	v_fmamk_f32 v19, v19, 0x3e0293ee, v34
	v_fmamk_f32 v20, v20, 0x3e0293ee, v34
	v_fmamk_f32 v21, v21, 0x3e0293ee, v34
	v_fmamk_f32 v22, v22, 0x3e0293ee, v34
	v_fmamk_f32 v23, v23, 0x3e0293ee, v34
	v_fmamk_f32 v24, v24, 0x3e0293ee, v34
	v_fmamk_f32 v25, v25, 0x3e0293ee, v34
	v_fmamk_f32 v26, v26, 0x3e0293ee, v34
	v_fmamk_f32 v27, v27, 0x3e0293ee, v34
	v_fmamk_f32 v28, v28, 0x3e0293ee, v34
	v_fmamk_f32 v29, v29, 0x3e0293ee, v34
	v_fmamk_f32 v30, v30, 0x3e0293ee, v34
	v_fmamk_f32 v31, v31, 0x3e0293ee, v34
	v_fmamk_f32 v32, v32, 0x3e0293ee, v34
	v_fmamk_f32 v33, v33, 0x3e0293ee, v34
	v_exp_f32_e32 v99, v19
	v_exp_f32_e32 v100, v20
	v_exp_f32_e32 v101, v21
	v_exp_f32_e32 v102, v22
	v_exp_f32_e32 v103, v23
	v_exp_f32_e32 v104, v24
	v_exp_f32_e32 v105, v25
	v_exp_f32_e32 v106, v26
	v_exp_f32_e32 v107, v27
	v_exp_f32_e32 v108, v28
	v_exp_f32_e32 v109, v29
	v_exp_f32_e32 v110, v30
	v_exp_f32_e32 v111, v31
	v_exp_f32_e32 v112, v32
	v_exp_f32_e32 v113, v33
	v_cndmask_b32_e64 v216, v18, 1.0, s[0:1]
	s_lshl_b32 s0, s42, 9
	s_add_i32 s0, s0, 0
	s_add_i32 s0, s0, 0x10000
	v_fma_f32 v128, v16, s14, v34
	v_fma_f32 v129, v17, s14, v34
	v_fma_f32 v126, v14, s14, v34
	v_fma_f32 v127, v15, s14, v34
	v_fma_f32 v124, v12, s14, v34
	v_fma_f32 v125, v13, s14, v34
	v_fma_f32 v122, v10, s14, v34
	v_fma_f32 v123, v11, s14, v34
	v_fma_f32 v120, v8, s14, v34
	v_fma_f32 v121, v9, s14, v34
	v_fma_f32 v118, v6, s14, v34
	v_fma_f32 v119, v7, s14, v34
	v_fma_f32 v116, v4, s14, v34
	v_fma_f32 v117, v5, s14, v34
	v_fma_f32 v114, v2, s14, v34
	v_fma_f32 v115, v3, s14, v34
	s_cmp_lt_i32 s56, 3
	v_lshl_add_u32 v211, v1, 2, s0
	v_lshl_add_u32 v210, v199, 2, s0
	s_waitcnt lgkmcnt(0)
	s_barrier
	s_cbranch_scc1 .LBB0_1897
	v_add_u32_e32 v2, s43, v204
	s_lshl_b32 s0, s56, 17
	v_mov_b32_e32 v217, 0
	s_mov_b32 s12, 2
	v_subrev_u32_e32 v219, s40, v2
	s_add_i32 s58, s40, 0xffffff7f
	s_add_i32 s38, s0, 0xfff60000
	v_mov_b32_e32 v50, 0
	v_mov_b32_e32 v51, v217
	v_mov_b32_e32 v52, v217
	v_mov_b32_e32 v53, v217
	v_mov_b32_e32 v54, v217
	v_mov_b32_e32 v55, v217
	v_mov_b32_e32 v56, v217
	v_mov_b32_e32 v57, v217
	v_mov_b32_e32 v58, v217
	v_mov_b32_e32 v59, v217
	v_mov_b32_e32 v60, v217
	v_mov_b32_e32 v61, v217
	v_mov_b32_e32 v62, v217
	v_mov_b32_e32 v63, v217
	v_mov_b32_e32 v64, v217
	v_mov_b32_e32 v65, v217
	v_mov_b32_e32 v34, 0
	v_mov_b32_e32 v35, v217
	v_mov_b32_e32 v36, v217
	v_mov_b32_e32 v37, v217
	v_mov_b32_e32 v38, v217
	v_mov_b32_e32 v39, v217
	v_mov_b32_e32 v40, v217
	v_mov_b32_e32 v41, v217
	v_mov_b32_e32 v42, v217
	v_mov_b32_e32 v43, v217
	v_mov_b32_e32 v44, v217
	v_mov_b32_e32 v45, v217
	v_mov_b32_e32 v46, v217
	v_mov_b32_e32 v47, v217
	v_mov_b32_e32 v48, v217
	v_mov_b32_e32 v49, v217
	v_mov_b32_e32 v18, 0
	v_mov_b32_e32 v19, v217
	v_mov_b32_e32 v20, v217
	v_mov_b32_e32 v21, v217
	v_mov_b32_e32 v22, v217
	v_mov_b32_e32 v23, v217
	v_mov_b32_e32 v24, v217
	v_mov_b32_e32 v25, v217
	v_mov_b32_e32 v26, v217
	v_mov_b32_e32 v27, v217
	v_mov_b32_e32 v28, v217
	v_mov_b32_e32 v29, v217
	v_mov_b32_e32 v30, v217
	v_mov_b32_e32 v31, v217
	v_mov_b32_e32 v32, v217
	v_mov_b32_e32 v33, v217
	v_mov_b32_e32 v2, 0
	v_mov_b32_e32 v3, v217
	v_mov_b32_e32 v4, v217
	v_mov_b32_e32 v5, v217
	v_mov_b32_e32 v6, v217
	v_mov_b32_e32 v7, v217
	v_mov_b32_e32 v8, v217
	v_mov_b32_e32 v9, v217
	v_mov_b32_e32 v10, v217
	v_mov_b32_e32 v11, v217
	v_mov_b32_e32 v12, v217
	v_mov_b32_e32 v13, v217
	v_mov_b32_e32 v14, v217
	v_mov_b32_e32 v15, v217
	v_mov_b32_e32 v16, v217
	v_mov_b32_e32 v17, v217
	s_branch .LBB0_1870

.LBB0_1872:
	ds_read_b64_tr_b16 v[110:111], v201 offset:0
	ds_read_b64_tr_b16 v[112:113], v201 offset:0x800
	ds_read_b64_tr_b16 v[118:119], v201 offset:0x1000
	ds_read_b64_tr_b16 v[120:121], v201 offset:0x1800
	ds_read_b64_tr_b16 v[122:123], v201 offset:0x2000
	ds_read_b64_tr_b16 v[124:125], v201 offset:0x2800
	ds_read_b64_tr_b16 v[126:127], v201 offset:0x3000
	ds_read_b64_tr_b16 v[128:129], v201 offset:0x3800
	s_waitcnt lgkmcnt(0)
	s_nop 0
	v_mfma_f32_32x32x16_bf16 v[50:65], v[114:117], v[110:113], v[50:65]
	v_max_f32_e32 v190, v67, v67
	v_max_f32_e32 v191, v66, v66
	v_max_f32_e32 v190, v191, v190
	v_max3_f32 v190, v190, v68, v69
	v_max3_f32 v190, v190, v70, v71
	ds_read_b64_tr_b16 v[178:179], v201 offset:0x200
	ds_read_b64_tr_b16 v[180:181], v201 offset:0xa00
	v_mfma_f32_32x32x16_bf16 v[50:65], v[106:109], v[118:121], v[50:65]
	v_max3_f32 v118, v190, v72, v73
	v_max3_f32 v118, v118, v74, v75
	v_max3_f32 v118, v118, v76, v77
	v_max3_f32 v118, v118, v78, v79
	v_max3_f32 v118, v118, v80, v81
	v_max3_f32 v118, v118, v82, v83
	v_max3_f32 v118, v118, v84, v85
	v_mfma_f32_32x32x16_bf16 v[50:65], v[102:105], v[122:125], v[50:65]
	ds_read_b64_tr_b16 v[182:183], v201 offset:0x1200
	v_max3_f32 v118, v118, v86, v87
	ds_read_b64_tr_b16 v[184:185], v201 offset:0x1a00
	v_max3_f32 v118, v118, v88, v89
	ds_read_b64_tr_b16 v[186:187], v201 offset:0x2200
	v_max3_f32 v118, v118, v90, v91
	ds_read_b64_tr_b16 v[188:189], v201 offset:0x2a00
	v_mfma_f32_32x32x16_bf16 v[50:65], v[98:101], v[126:129], v[50:65]
	v_max3_f32 v118, v118, v92, v93
	ds_read_b64_tr_b16 v[110:111], v201 offset:0x3200
	v_max3_f32 v118, v118, v94, v95
	ds_read_b64_tr_b16 v[112:113], v201 offset:0x3a00
	v_max3_f32 v118, v118, v96, v97
	v_mov_b32_e32 v119, v118
	s_waitcnt lgkmcnt(0)
	s_nop 1
	v_permlane32_swap_b32_e32 v118, v119
	v_max_f32_e32 v119, v119, v119
	v_max_f32_e32 v118, v118, v118
	v_max_f32_e32 v190, v118, v119
	v_mfma_f32_32x32x16_bf16 v[34:49], v[114:117], v[178:181], v[34:49]
	v_sub_f32_e32 v191, v190, v215
	ds_read_b64_tr_b16 v[118:119], v201 offset:0x400
	v_mul_f32_e32 v191, 0x3db504f3, v191
	ds_read_b64_tr_b16 v[120:121], v201 offset:0xc00
	v_cmp_ge_f32_e32 vcc, s51, v191
	ds_read_b64_tr_b16 v[122:123], v201 offset:0x1400
	s_cmp_eq_u64 vcc, exec
	v_mfma_f32_32x32x16_bf16 v[34:49], v[106:109], v[182:185], v[34:49]
	v_max_f32_e32 v191, v215, v215
	ds_read_b64_tr_b16 v[124:125], v201 offset:0x1c00
	v_max_f32_e32 v182, v191, v190
	s_cselect_b64 vcc, -1, 0
	ds_read_b64_tr_b16 v[126:127], v201 offset:0x2400
	v_cndmask_b32_e32 v223, v182, v215, vcc
	ds_read_b64_tr_b16 v[128:129], v201 offset:0x2c00
	v_mfma_f32_32x32x16_bf16 v[34:49], v[102:105], v[186:189], v[34:49]
	v_mul_f32_e32 v182, 0xbe0293ee, v223
	ds_read_b64_tr_b16 v[178:179], v201 offset:0x3400
	v_fma_f32 v80, v80, s14, v182
	v_fma_f32 v81, v81, s14, v182
	v_fma_f32 v78, v78, s14, v182
	v_fma_f32 v79, v79, s14, v182
	v_fma_f32 v76, v76, s14, v182
	v_fma_f32 v77, v77, s14, v182
	v_fma_f32 v74, v74, s14, v182
	v_fma_f32 v75, v75, s14, v182
	v_fma_f32 v72, v72, s14, v182
	v_fma_f32 v73, v73, s14, v182
	v_mfma_f32_32x32x16_bf16 v[34:49], v[98:101], v[110:113], v[34:49]
	v_fma_f32 v70, v70, s14, v182
	v_fma_f32 v71, v71, s14, v182
	v_fma_f32 v68, v68, s14, v182
	v_fma_f32 v69, v69, s14, v182
	v_fma_f32 v66, v66, s14, v182
	v_fma_f32 v67, v67, s14, v182
	v_fma_f32 v96, v96, s14, v182
	v_fma_f32 v97, v97, s14, v182
	v_fma_f32 v94, v94, s14, v182
	v_fma_f32 v95, v95, s14, v182
	v_fma_f32 v92, v92, s14, v182
	v_fma_f32 v93, v93, s14, v182
	v_fma_f32 v90, v90, s14, v182
	v_fma_f32 v91, v91, s14, v182
	v_fma_f32 v88, v88, s14, v182
	v_fma_f32 v89, v89, s14, v182
	v_fma_f32 v86, v86, s14, v182
	v_fma_f32 v87, v87, s14, v182
	v_fma_f32 v84, v84, s14, v182
	v_fma_f32 v85, v85, s14, v182
	v_fma_f32 v82, v82, s14, v182
	v_fma_f32 v83, v83, s14, v182
	ds_read_b64_tr_b16 v[180:181], v201 offset:0x3c00
	s_nop 0
	s_waitcnt lgkmcnt(0)
	v_mfma_f32_32x32x16_bf16 v[18:33], v[114:117], v[118:121], v[18:33]
	ds_read_b64_tr_b16 v[110:111], v201 offset:0x600
	ds_read_b64_tr_b16 v[112:113], v201 offset:0xe00
	ds_read_b64_tr_b16 v[118:119], v201 offset:0x1600
	ds_read_b64_tr_b16 v[120:121], v201 offset:0x1e00
	v_exp_f32_e32 v66, v66
	v_exp_f32_e32 v67, v67
	v_exp_f32_e32 v68, v68
	v_mfma_f32_32x32x16_bf16 v[18:33], v[106:109], v[122:125], v[18:33]
	ds_read_b64_tr_b16 v[122:123], v201 offset:0x2600
	ds_read_b64_tr_b16 v[124:125], v201 offset:0x2e00
	v_exp_f32_e32 v69, v69
	v_exp_f32_e32 v70, v70
	v_exp_f32_e32 v71, v71
	v_exp_f32_e32 v72, v72
	v_exp_f32_e32 v73, v73
	v_mfma_f32_32x32x16_bf16 v[18:33], v[102:105], v[126:129], v[18:33]
	ds_read_b64_tr_b16 v[126:127], v201 offset:0x3600
	ds_read_b64_tr_b16 v[128:129], v201 offset:0x3e00
	s_waitcnt lgkmcnt(0)
	v_mfma_f32_32x32x16_bf16 v[18:33], v[98:101], v[178:181], v[18:33]
	v_mfma_f32_32x32x16_bf16 v[2:17], v[114:117], v[110:113], v[2:17]
	v_exp_f32_e32 v74, v74
	v_exp_f32_e32 v75, v75
	v_exp_f32_e32 v76, v76
	v_exp_f32_e32 v77, v77
	v_exp_f32_e32 v78, v78
	v_exp_f32_e32 v79, v79
	v_exp_f32_e32 v80, v80
	v_mfma_f32_32x32x16_bf16 v[2:17], v[106:109], v[118:121], v[2:17]
	v_exp_f32_e32 v81, v81
	s_waitcnt vmcnt(2)
	ds_write_b128 v208, v[170:173] offset:32768
	ds_write_b128 v208, v[174:177] offset:40960
	v_mfma_f32_32x32x16_bf16 v[2:17], v[102:105], v[122:125], v[2:17]
	v_mfma_f32_32x32x16_bf16 v[2:17], v[98:101], v[126:129], v[2:17]
	s_mov_b64 s[0:1], exec
	v_readlane_b32 s40, v254, 7
	v_readlane_b32 s41, v254, 8
	s_and_b64 s[40:41], s[0:1], s[40:41]
	s_mov_b64 exec, s[40:41]
	v_add_u32_e32 v99, 0, v198
	v_xor_b32_e32 v98, 0x80000000, v197
	v_add_u32_e32 v99, 0x11000, v99
	ds_write_b32 v99, v98
	s_or_b64 exec, exec, s[0:1]
	s_add_i32 s0, s12, 1
	s_cmp_lt_i32 s0, s56
	s_cselect_b64 s[40:41], -1, 0
	s_cmp_ge_i32 s0, s56
	s_cbranch_scc1 .LBB0_1878
	s_add_i32 s0, s38, 0x20000
	s_ashr_i32 s1, s0, 31
	s_lshl_b64 s[0:1], s[0:1], 1
	s_add_u32 s0, s30, s0
	s_addc_u32 s1, s31, s1
	v_lshl_add_u64 v[98:99], s[0:1], 0, v[194:195]
	v_add_co_u32_e32 v98, vcc, 0x20000, v98
	s_nop 1
	v_addc_co_u32_e32 v99, vcc, 0, v99, vcc
	global_load_dwordx4 v[170:173], v194, s[0:1]
	global_load_dwordx4 v[174:177], v[98:99], off
	s_mov_b64 s[0:1], exec
	v_readlane_b32 s60, v254, 7
	v_readlane_b32 s61, v254, 8
	s_and_b64 s[60:61], s[0:1], s[60:61]
	s_mov_b64 exec, s[60:61]
	s_cbranch_execz .LBB0_1877
	v_add_u32_e32 v98, s58, v0
	v_add_u32_e32 v98, 0xffffff81, v98
	v_ashrrev_i32_e32 v99, 31, v98
	v_lshl_add_u64 v[98:99], v[98:99], 2, s[34:35]
	global_load_dword v197, v[98:99], off

.LBB0_1886:
	ds_read_b64_tr_b16 v[226:227], v201 offset:0x4000
	ds_read_b64_tr_b16 v[228:229], v201 offset:0x4800
	ds_read_b64_tr_b16 v[230:231], v201 offset:0x5000
	ds_read_b64_tr_b16 v[232:233], v201 offset:0x5800
	ds_read_b64_tr_b16 v[234:235], v201 offset:0x6000
	ds_read_b64_tr_b16 v[236:237], v201 offset:0x6800
	ds_read_b64_tr_b16 v[238:239], v201 offset:0x7000
	ds_read_b64_tr_b16 v[240:241], v201 offset:0x7800
	s_waitcnt lgkmcnt(0)
	s_nop 0
	v_mfma_f32_32x32x16_bf16 v[50:65], v[186:189], v[226:229], v[50:65]
	v_max_f32_e32 v214, v99, v99
	v_max_f32_e32 v215, v98, v98
	v_max_f32_e32 v214, v215, v214
	v_max3_f32 v214, v214, v100, v101
	v_max3_f32 v214, v214, v102, v103
	v_max3_f32 v214, v214, v104, v105
	v_max3_f32 v214, v214, v106, v107
	v_mfma_f32_32x32x16_bf16 v[50:65], v[190:193], v[230:233], v[50:65]
	v_max3_f32 v214, v214, v108, v109
	v_max3_f32 v214, v214, v110, v111
	v_max3_f32 v214, v214, v112, v113
	ds_read_b64_tr_b16 v[242:243], v201 offset:0x4200
	v_max3_f32 v214, v214, v114, v115
	ds_read_b64_tr_b16 v[244:245], v201 offset:0x4a00
	v_max3_f32 v214, v214, v116, v117
	v_mfma_f32_32x32x16_bf16 v[50:65], v[182:185], v[234:237], v[50:65]
	ds_read_b64_tr_b16 v[246:247], v201 offset:0x5200
	v_max3_f32 v214, v214, v118, v119
	ds_read_b64_tr_b16 v[248:249], v201 offset:0x5a00
	v_max3_f32 v214, v214, v120, v121
	ds_read_b64_tr_b16 v[250:251], v201 offset:0x6200
	v_max3_f32 v214, v214, v122, v123
	ds_read_b64_tr_b16 v[252:253], v201 offset:0x6a00
	v_mfma_f32_32x32x16_bf16 v[50:65], v[178:181], v[238:241], v[50:65]
	v_max3_f32 v214, v214, v124, v125
	ds_read_b64_tr_b16 v[226:227], v201 offset:0x7200
	v_max3_f32 v214, v214, v126, v127
	ds_read_b64_tr_b16 v[228:229], v201 offset:0x7a00
	v_max3_f32 v214, v214, v128, v129
	v_mov_b32_e32 v215, v214
	s_waitcnt lgkmcnt(0)
	s_nop 1
	v_permlane32_swap_b32_e32 v214, v215
	v_max_f32_e32 v215, v215, v215
	v_max_f32_e32 v214, v214, v214
	v_max_f32_e32 v214, v214, v215
	v_mfma_f32_32x32x16_bf16 v[34:49], v[186:189], v[242:245], v[34:49]
	v_sub_f32_e32 v215, v214, v223
	ds_read_b64_tr_b16 v[230:231], v201 offset:0x4400
	v_mul_f32_e32 v215, 0x3db504f3, v215
	ds_read_b64_tr_b16 v[232:233], v201 offset:0x4c00
	v_cmp_ge_f32_e32 vcc, s51, v215
	ds_read_b64_tr_b16 v[234:235], v201 offset:0x5400
	s_cmp_eq_u64 vcc, exec
	v_mfma_f32_32x32x16_bf16 v[34:49], v[190:193], v[246:249], v[34:49]
	v_max_f32_e32 v215, v223, v223
	ds_read_b64_tr_b16 v[236:237], v201 offset:0x5c00
	v_max_f32_e32 v214, v215, v214
	s_cselect_b64 vcc, -1, 0
	ds_read_b64_tr_b16 v[238:239], v201 offset:0x6400
	v_cndmask_b32_e32 v215, v214, v223, vcc
	ds_read_b64_tr_b16 v[240:241], v201 offset:0x6c00
	v_mfma_f32_32x32x16_bf16 v[34:49], v[182:185], v[250:253], v[34:49]
	v_mul_f32_e32 v214, 0xbe0293ee, v215
	ds_read_b64_tr_b16 v[242:243], v201 offset:0x7400
	v_fma_f32 v112, v112, s14, v214
	v_fma_f32 v113, v113, s14, v214
	v_fma_f32 v110, v110, s14, v214
	v_fma_f32 v111, v111, s14, v214
	v_fma_f32 v108, v108, s14, v214
	v_fma_f32 v109, v109, s14, v214
	v_fma_f32 v106, v106, s14, v214
	v_fma_f32 v107, v107, s14, v214
	v_fma_f32 v104, v104, s14, v214
	v_fma_f32 v105, v105, s14, v214
	v_mfma_f32_32x32x16_bf16 v[34:49], v[178:181], v[226:229], v[34:49]
	v_fma_f32 v102, v102, s14, v214
	v_fma_f32 v103, v103, s14, v214
	v_fma_f32 v100, v100, s14, v214
	v_fma_f32 v101, v101, s14, v214
	v_fma_f32 v98, v98, s14, v214
	v_fma_f32 v99, v99, s14, v214
	v_fma_f32 v128, v128, s14, v214
	v_fma_f32 v129, v129, s14, v214
	v_fma_f32 v126, v126, s14, v214
	v_fma_f32 v127, v127, s14, v214
	v_fma_f32 v124, v124, s14, v214
	v_fma_f32 v125, v125, s14, v214
	v_fma_f32 v122, v122, s14, v214
	v_fma_f32 v123, v123, s14, v214
	v_fma_f32 v120, v120, s14, v214
	v_fma_f32 v121, v121, s14, v214
	v_fma_f32 v118, v118, s14, v214
	v_fma_f32 v119, v119, s14, v214
	v_fma_f32 v116, v116, s14, v214
	v_fma_f32 v117, v117, s14, v214
	v_fma_f32 v114, v114, s14, v214
	v_fma_f32 v115, v115, s14, v214
	ds_read_b64_tr_b16 v[244:245], v201 offset:0x7c00
	s_nop 0
	s_waitcnt lgkmcnt(0)
	v_mfma_f32_32x32x16_bf16 v[18:33], v[186:189], v[230:233], v[18:33]
	ds_read_b64_tr_b16 v[226:227], v201 offset:0x4600
	ds_read_b64_tr_b16 v[228:229], v201 offset:0x4e00
	ds_read_b64_tr_b16 v[230:231], v201 offset:0x5600
	ds_read_b64_tr_b16 v[232:233], v201 offset:0x5e00
	v_exp_f32_e32 v98, v98
	v_exp_f32_e32 v99, v99
	v_exp_f32_e32 v100, v100
	v_mfma_f32_32x32x16_bf16 v[18:33], v[190:193], v[234:237], v[18:33]
	ds_read_b64_tr_b16 v[234:235], v201 offset:0x6600
	ds_read_b64_tr_b16 v[236:237], v201 offset:0x6e00
	v_exp_f32_e32 v101, v101
	v_exp_f32_e32 v102, v102
	v_exp_f32_e32 v103, v103
	v_exp_f32_e32 v104, v104
	v_exp_f32_e32 v105, v105
	v_mfma_f32_32x32x16_bf16 v[18:33], v[182:185], v[238:241], v[18:33]
	ds_read_b64_tr_b16 v[238:239], v201 offset:0x7600
	ds_read_b64_tr_b16 v[240:241], v201 offset:0x7e00
	s_waitcnt lgkmcnt(0)
	v_mfma_f32_32x32x16_bf16 v[18:33], v[178:181], v[242:245], v[18:33]
	v_mfma_f32_32x32x16_bf16 v[2:17], v[186:189], v[226:229], v[2:17]
	v_exp_f32_e32 v106, v106
	v_exp_f32_e32 v107, v107
	v_exp_f32_e32 v108, v108
	v_exp_f32_e32 v109, v109
	v_exp_f32_e32 v110, v110
	v_exp_f32_e32 v111, v111
	v_exp_f32_e32 v112, v112
	v_mfma_f32_32x32x16_bf16 v[2:17], v[190:193], v[230:233], v[2:17]
	v_exp_f32_e32 v113, v113
	s_and_b64 vcc, exec, s[0:1]
	v_mfma_f32_32x32x16_bf16 v[2:17], v[182:185], v[234:237], v[2:17]
	v_mfma_f32_32x32x16_bf16 v[2:17], v[178:181], v[238:241], v[2:17]
	s_cbranch_vccnz .LBB0_1890
	s_waitcnt vmcnt(2)
	ds_write_b128 v208, v[170:173] offset:49152
	ds_write_b128 v208, v[174:177] offset:57344
	s_mov_b64 s[0:1], exec
	v_readlane_b32 s40, v254, 7
	v_readlane_b32 s41, v254, 8
	s_and_b64 s[40:41], s[0:1], s[40:41]
	s_mov_b64 exec, s[40:41]
	v_add_u32_e32 v179, 0, v198
	v_xor_b32_e32 v178, 0x80000000, v197
	v_add_u32_e32 v179, 0x11100, v179
	ds_write_b32 v179, v178
	s_or_b64 exec, exec, s[0:1]
